# speedup vs baseline: 1.0174x; 1.0174x over previous
_Z11attn_kernelPKDF16_S0_PDF16_P15HIP_vector_typeIfLj2EE:
	s_getpc_b64 s[38:39]
	v_lshlrev_b32_e32 v240, 7, v0
	v_min_u32_e32 v240, 0x3380, v240
	global_load_dword v241, v240, s[38:39]
	s_mov_b32 s5, 0
	s_mov_b32 s28, s3
	s_load_dwordx8 s[20:27], s[0:1], 0x0
	s_mov_b32 s3, s5
	s_lshl_b64 s[0:1], s[4:5], 12
	s_lshl_b64 s[2:3], s[2:3], 8
	s_add_u32 s0, s0, s2
	v_lshrrev_b32_e32 v1, 6, v0
	s_addc_u32 s1, s1, s3
	v_and_b32_e32 v160, 31, v0
	s_lshl_b64 s[2:3], s[0:1], 8
	v_lshlrev_b32_e32 v162, 5, v1
	s_waitcnt lgkmcnt(0)
	s_add_u32 s2, s20, s2
	v_or_b32_e32 v2, v162, v160
	v_bfe_u32 v54, v0, 5, 1
	s_addc_u32 s3, s21, s3
	v_and_b32_e32 v164, 63, v0
	v_lshrrev_b32_e32 v165, 4, v164
	v_add_u32_e32 v165, v162, v165
	v_lshlrev_b32_e32 v165, 8, v165
	v_and_b32_e32 v164, 15, v164
	v_lshl_add_u32 v164, v164, 4, v165
	v_mov_b32_e32 v165, 0
	v_lshl_add_u64 v[2:3], s[2:3], 0, v[164:165]
	s_mov_b64 s[6:7], 0x1000
	v_lshl_add_u64 v[4:5], v[2:3], 0, s[6:7]
	global_load_dwordx4 v[156:159], v[2:3], off
	global_load_dwordx4 v[152:155], v[2:3], off offset:1024
	global_load_dwordx4 v[148:151], v[2:3], off offset:2048
	global_load_dwordx4 v[144:147], v[2:3], off offset:3072
	global_load_dwordx4 v[140:143], v[4:5], off
	global_load_dwordx4 v[136:139], v[4:5], off offset:1024
	global_load_dwordx4 v[132:135], v[4:5], off offset:2048
	global_load_dwordx4 v[128:131], v[4:5], off offset:3072
	v_lshlrev_b32_e32 v164, 4, v54
	s_ashr_i32 s29, s28, 31
	v_bfe_u32 v55, v0, 2, 3
	s_lshl_b64 s[2:3], s[4:5], 20
	s_lshl_b64 s[20:21], s[28:29], 18
	v_lshl_or_b32 v2, v1, 3, v55
	s_add_u32 s4, s22, s2
	v_lshrrev_b32_e32 v3, 2, v2
	s_addc_u32 s7, s23, s3
	v_xor_b32_e32 v4, v3, v0
	s_add_u32 s6, s4, s20
	v_and_b32_e32 v5, 32, v0
	v_lshlrev_b32_e32 v4, 3, v4
	v_lshlrev_b32_e32 v1, 11, v1
	s_addc_u32 s7, s7, s21
	v_lshlrev_b32_e32 v164, 8, v2
	v_and_or_b32 v4, v4, 24, v5
	v_add_u32_e32 v173, 0, v1
	v_lshl_add_u64 v[2:3], s[6:7], 0, v[164:165]
	v_lshlrev_b32_e32 v164, 1, v4
	v_readfirstlane_b32 s4, v173
	v_add_u32_e32 v6, 0x400, v173
	v_lshl_add_u64 v[2:3], v[2:3], 0, v[164:165]
	s_mov_b64 s[6:7], 0x80
	s_mov_b32 m0, s4
	v_readfirstlane_b32 s4, v6
	v_add_u32_e32 v6, 0x4000, v173
	v_lshl_add_u64 v[4:5], v[2:3], 0, s[6:7]
	global_load_lds_dwordx4 v[2:3], off
	s_mov_b32 m0, s4
	s_mov_b64 s[6:7], 0x4000
	v_readfirstlane_b32 s4, v6
	global_load_lds_dwordx4 v[4:5], off
	v_lshl_add_u64 v[4:5], v[2:3], 0, s[6:7]
	s_mov_b32 m0, s4
	s_mov_b64 s[6:7], 0x4080
	global_load_lds_dwordx4 v[4:5], off
	v_add_u32_e32 v4, 0x4400, v173
	v_lshl_add_u64 v[2:3], v[2:3], 0, s[6:7]
	v_readfirstlane_b32 s4, v4
	s_mov_b32 m0, s4
	s_movk_i32 s4, 0x1c0
	global_load_lds_dwordx4 v[2:3], off
	v_lshlrev_b32_e32 v2, 8, v0
	v_and_b32_e32 v2, 0x1800, v2
	v_lshlrev_b32_e32 v3, 6, v0
	v_and_or_b32 v6, v3, s4, v2
	v_xor_b32_e32 v2, v54, v55
	v_lshlrev_b32_e32 v2, 4, v2
	v_and_or_b32 v175, v2, 48, v6
	v_and_b32_e32 v190, 63, v0
	v_lshrrev_b32_e32 v191, 4, v190
	v_and_b32_e32 v192, 15, v190
	v_xor_b32_e32 v193, v192, v191
	v_lshlrev_b32_e32 v193, 4, v193
	v_add_u32_e32 v194, v162, v191
	v_lshlrev_b32_e32 v194, 8, v194
	v_add_u32_e32 v194, 0x10000, v194
	v_and_b32_e32 v195, 15, v160
	v_xor_b32_e32 v195, v195, v54
	v_lshlrev_b32_e32 v195, 4, v195
	v_add_u32_e32 v196, v162, v160
	v_lshlrev_b32_e32 v196, 8, v196
	v_add_u32_e32 v196, 0x10000, v196
	s_waitcnt vmcnt(4)
	v_xor_b32_e32 v197, 0x0, v193
	v_add_u32_e32 v197, v197, v194
	ds_write_b128 v197, v[156:159] offset:0
	v_xor_b32_e32 v197, 0x40, v193
	v_add_u32_e32 v197, v197, v194
	ds_write_b128 v197, v[152:155] offset:1024
	v_xor_b32_e32 v197, 0x80, v193
	v_add_u32_e32 v197, v197, v194
	ds_write_b128 v197, v[148:151] offset:2048
	v_xor_b32_e32 v197, 0xc0, v193
	v_add_u32_e32 v197, v197, v194
	ds_write_b128 v197, v[144:147] offset:3072
	v_xor_b32_e32 v197, 0x0, v193
	v_add_u32_e32 v197, v197, v194
	ds_write_b128 v197, v[140:143] offset:4096
	v_xor_b32_e32 v197, 0x40, v193
	v_add_u32_e32 v197, v197, v194
	ds_write_b128 v197, v[136:139] offset:5120
	v_xor_b32_e32 v197, 0x80, v193
	v_add_u32_e32 v197, v197, v194
	ds_write_b128 v197, v[132:135] offset:6144
	v_xor_b32_e32 v197, 0xc0, v193
	v_add_u32_e32 v197, v197, v194
	ds_write_b128 v197, v[128:131] offset:7168
	s_waitcnt lgkmcnt(0)
	v_xor_b32_e32 v198, 0x0, v195
	v_add_u32_e32 v198, v198, v196
	ds_read_b128 v[156:159], v198
	v_xor_b32_e32 v198, 0x20, v195
	v_add_u32_e32 v198, v198, v196
	ds_read_b128 v[152:155], v198
	v_xor_b32_e32 v198, 0x40, v195
	v_add_u32_e32 v198, v198, v196
	ds_read_b128 v[148:151], v198
	v_xor_b32_e32 v198, 0x60, v195
	v_add_u32_e32 v198, v198, v196
	ds_read_b128 v[144:147], v198
	v_xor_b32_e32 v198, 0x80, v195
	v_add_u32_e32 v198, v198, v196
	ds_read_b128 v[140:143], v198
	v_xor_b32_e32 v198, 0xa0, v195
	v_add_u32_e32 v198, v198, v196
	ds_read_b128 v[136:139], v198
	v_xor_b32_e32 v198, 0xc0, v195
	v_add_u32_e32 v198, v198, v196
	ds_read_b128 v[132:135], v198
	v_xor_b32_e32 v198, 0xe0, v195
	v_add_u32_e32 v198, v198, v196
	ds_read_b128 v[128:131], v198
	s_waitcnt vmcnt(2)
	v_add_u32_e32 v172, 0, v175
	s_waitcnt lgkmcnt(0)
	s_barrier
	ds_read_b128 v[2:5], v172
	ds_read_b128 v[34:37], v172 offset:512
	v_bitop3_b32 v7, v54, v55, 2 bitop3:0x36
	v_lshlrev_b32_e32 v7, 4, v7
	v_and_or_b32 v176, v7, 48, v6
	v_add_u32_e32 v174, 0, v176
	ds_read_b128 v[18:21], v174
	ds_read_b128 v[38:41], v174 offset:512
	s_mov_b32 s33, 0x41200000
	s_cmp_lg_u32 0, -1
	s_cselect_b32 s37, 0, 0
	s_waitcnt vmcnt(2) lgkmcnt(0)
	v_mfma_f32_32x32x16_f16 v[2:17], v[2:5], v[156:159], 0
	s_movk_i32 s4, 0x110
	v_and_b32_e32 v161, 63, v0
	v_lshl_or_b32 v1, v55, 8, v1
	s_mov_b32 s18, s5
	s_mov_b32 s19, s5
	s_mov_b32 s6, s5
	s_mov_b32 s7, s5
	v_mfma_f32_32x32x16_f16 v[2:17], v[18:21], v[152:155], v[2:17]
	ds_read_b128 v[18:21], v172 offset:8192
	ds_read_b128 v[42:45], v172 offset:8704
	ds_read_b128 v[46:49], v174 offset:8192
	ds_read_b128 v[50:53], v174 offset:8704
	s_mov_b32 s8, s5
	s_mov_b32 s9, s5
	s_mov_b32 s10, s5
	s_mov_b32 s11, s5
	s_mov_b32 s12, s5
	s_waitcnt lgkmcnt(3)
	v_mfma_f32_32x32x16_f16 v[18:33], v[18:21], v[156:159], 0
	s_mov_b32 s13, s5
	s_mov_b32 s14, s5
	s_mov_b32 s15, s5
	s_mov_b32 s16, s5
	s_mov_b32 s17, s5
	s_mov_b32 s36, 1
	s_mov_b32 s34, -1
	s_waitcnt lgkmcnt(1)
	v_mfma_f32_32x32x16_f16 v[18:33], v[46:49], v[152:155], v[18:33]
	s_mov_b32 s35, 2
	s_mov_b64 s[30:31], 0x8000
	v_mfma_f32_32x32x16_f16 v[2:17], v[34:37], v[148:151], v[2:17]
	v_mfma_f32_32x32x16_f16 v[18:33], v[42:45], v[148:151], v[18:33]
	v_mfma_f32_32x32x16_f16 v[2:17], v[38:41], v[144:147], v[2:17]
	ds_read_b128 v[34:37], v172 offset:1024
	ds_read_b128 v[38:41], v172 offset:1536
	s_waitcnt lgkmcnt(2)
	v_mfma_f32_32x32x16_f16 v[18:33], v[50:53], v[144:147], v[18:33]
	s_waitcnt lgkmcnt(1)
	v_mfma_f32_32x32x16_f16 v[2:17], v[34:37], v[140:143], v[2:17]
	ds_read_b128 v[34:37], v172 offset:9216
	ds_read_b128 v[42:45], v172 offset:9728
	s_waitcnt lgkmcnt(1)
	v_mfma_f32_32x32x16_f16 v[18:33], v[34:37], v[140:143], v[18:33]
	ds_read_b128 v[34:37], v174 offset:1024
	ds_read_b128 v[46:49], v174 offset:1536
	s_waitcnt lgkmcnt(1)
	v_mfma_f32_32x32x16_f16 v[2:17], v[34:37], v[136:139], v[2:17]
	ds_read_b128 v[34:37], v174 offset:9216
	ds_read_b128 v[50:53], v174 offset:9728
	v_mfma_f32_32x32x16_f16 v[2:17], v[38:41], v[132:135], v[2:17]
	s_waitcnt lgkmcnt(1)
	v_mfma_f32_32x32x16_f16 v[18:33], v[34:37], v[136:139], v[18:33]
	v_mov_b32_e32 v34, 0xf149f2ca
	v_mfma_f32_32x32x16_f16 v[2:17], v[46:49], v[128:131], v[2:17]
	v_mfma_f32_32x32x16_f16 v[18:33], v[42:45], v[132:135], v[18:33]
	s_nop 10
	v_max_f32_e32 v35, v3, v3
	v_max_f32_e32 v36, v2, v2
	v_max_f32_e32 v35, v36, v35
	v_max3_f32 v35, v35, v4, v5
	v_max3_f32 v35, v35, v6, v7
	v_max3_f32 v35, v35, v8, v9
	v_max3_f32 v35, v35, v10, v11
	s_waitcnt lgkmcnt(0)
	v_mfma_f32_32x32x16_f16 v[18:33], v[50:53], v[128:131], v[18:33]
	v_max3_f32 v35, v35, v12, v13
	v_max3_f32 v35, v35, v14, v15
	v_max3_f32 v35, v35, v16, v17
	s_nop 8
	v_max3_f32 v35, v35, v18, v19
	v_max3_f32 v35, v35, v20, v21
	v_max3_f32 v35, v35, v22, v23
	v_max3_f32 v35, v35, v24, v25
	v_max3_f32 v35, v35, v26, v27
	v_max3_f32 v35, v35, v28, v29
	v_max3_f32 v35, v35, v30, v31
	v_max3_f32 v35, v35, v32, v33
	v_mov_b32_e32 v36, v35
	s_nop 1
	v_permlane32_swap_b32_e32 v35, v36
	v_max_f32_e32 v36, v36, v36
	v_max_f32_e32 v35, v35, v35
	v_max_f32_e32 v35, v35, v36
	v_add_f32_e32 v36, 0x7149f2ca, v35
	v_cmp_ge_f32_e32 vcc, s33, v36
	s_cmp_eq_u64 vcc, exec
	v_max_f32_e32 v35, 0xf149f2ca, v35
	s_cselect_b64 vcc, -1, 0
	v_cndmask_b32_e32 v168, v35, v34, vcc
	v_sub_f32_e32 v96, v18, v168
	v_sub_f32_e32 v97, v19, v168
	v_lshlrev_b32_e32 v18, 4, v0
	v_lshrrev_b32_e32 v19, 4, v0
	v_sub_f32_e32 v98, v20, v168
	v_and_b32_e32 v18, 0xc0, v18
	v_bitop3_b32 v19, v19, v54, 1 bitop3:0x6c
	v_lshlrev_b32_e32 v20, 3, v0
	v_sub_f32_e32 v99, v21, v168
	v_lshl_or_b32 v18, v54, 11, v18
	v_lshlrev_b32_e32 v19, 5, v19
	v_and_b32_e32 v21, 8, v20
	v_or3_b32 v18, v18, v21, v19
	v_and_b32_e32 v19, 16, v20
	v_sub_f32_e32 v0, 0xf149f2ca, v35
	v_add3_u32 v163, v19, s37, v18
	v_bitop3_b32 v169, v18, s4, v19 bitop3:0x36
	v_exp_f32_e32 v18, v0
	s_add_u32 s2, s2, s20
	v_sub_f32_e32 v2, v2, v168
	v_sub_f32_e32 v3, v3, v168
	v_sub_f32_e32 v4, v4, v168
	v_sub_f32_e32 v5, v5, v168
	v_sub_f32_e32 v6, v6, v168
	v_sub_f32_e32 v7, v7, v168
	v_sub_f32_e32 v8, v8, v168
	v_sub_f32_e32 v9, v9, v168
	v_sub_f32_e32 v10, v10, v168
	v_sub_f32_e32 v11, v11, v168
	v_sub_f32_e32 v12, v12, v168
	v_sub_f32_e32 v13, v13, v168
	v_sub_f32_e32 v14, v14, v168
	v_sub_f32_e32 v15, v15, v168
	v_sub_f32_e32 v16, v16, v168
	v_sub_f32_e32 v17, v17, v168
	s_addc_u32 s3, s3, s21
	s_mov_b32 s4, s5
	v_exp_f32_e32 v127, v2
	v_exp_f32_e32 v180, v3
	v_exp_f32_e32 v125, v4
	v_exp_f32_e32 v179, v5
	v_exp_f32_e32 v123, v6
	v_exp_f32_e32 v126, v7
	v_exp_f32_e32 v122, v8
	v_exp_f32_e32 v124, v9
	v_exp_f32_e32 v119, v10
	v_exp_f32_e32 v121, v11
	v_exp_f32_e32 v117, v12
	v_exp_f32_e32 v120, v13
	v_exp_f32_e32 v115, v14
	v_exp_f32_e32 v118, v15
	v_exp_f32_e32 v114, v16
	v_exp_f32_e32 v116, v17
	v_or3_b32 v0, s2, v1, v164
	v_mov_b32_e32 v1, s3
	v_lshlrev_b32_e32 v164, 3, v54
	v_mov_b64_e32 v[62:63], s[18:19]
	v_lshl_add_u64 v[0:1], s[22:23], 0, v[0:1]
	s_mov_b64 s[2:3], 0xc080
	v_mov_b64_e32 v[48:49], s[4:5]
	v_sub_f32_e32 v100, v22, v168
	v_sub_f32_e32 v101, v23, v168
	v_sub_f32_e32 v102, v24, v168
	v_sub_f32_e32 v103, v25, v168
	v_sub_f32_e32 v104, v26, v168
	v_sub_f32_e32 v105, v27, v168
	v_sub_f32_e32 v106, v28, v168
	v_sub_f32_e32 v107, v29, v168
	v_sub_f32_e32 v108, v30, v168
	v_sub_f32_e32 v109, v31, v168
	v_sub_f32_e32 v110, v32, v168
	v_sub_f32_e32 v111, v33, v168
	v_lshl_add_u64 v[170:171], v[0:1], 0, s[2:3]
	s_movk_i32 s2, 0xbf80
	s_movk_i32 s20, 0xc000
	s_movk_i32 s22, 0xff80
	v_mov_b32_e32 v166, 1.0
	v_mov_b64_e32 v[60:61], s[16:17]
	v_mov_b64_e32 v[58:59], s[14:15]
	v_mov_b64_e32 v[56:57], s[12:13]
	v_mov_b64_e32 v[54:55], s[10:11]
	v_mov_b64_e32 v[52:53], s[8:9]
	v_mov_b64_e32 v[50:51], s[6:7]
	v_mov_b64_e32 v[32:33], v[48:49]
	v_mov_b64_e32 v[16:17], v[48:49]
	v_mov_b64_e32 v[0:1], v[48:49]
	s_mov_b32 s3, -1
	s_mov_b32 s21, -1
	s_mov_b32 s23, -1
	v_add_u32_e32 v167, s37, v169
	v_mov_b64_e32 v[34:35], v[50:51]
	v_mov_b64_e32 v[36:37], v[52:53]
	v_mov_b64_e32 v[38:39], v[54:55]
	v_mov_b64_e32 v[40:41], v[56:57]
	v_mov_b64_e32 v[42:43], v[58:59]
	v_mov_b64_e32 v[44:45], v[60:61]
	v_mov_b64_e32 v[46:47], v[62:63]
	v_mov_b64_e32 v[18:19], v[50:51]
	v_mov_b64_e32 v[20:21], v[52:53]
	v_mov_b64_e32 v[22:23], v[54:55]
	v_mov_b64_e32 v[24:25], v[56:57]
	v_mov_b64_e32 v[26:27], v[58:59]
	v_mov_b64_e32 v[28:29], v[60:61]
	v_mov_b64_e32 v[30:31], v[62:63]
	v_mov_b64_e32 v[2:3], v[50:51]
	v_mov_b64_e32 v[4:5], v[52:53]
	v_mov_b64_e32 v[6:7], v[54:55]
	v_mov_b64_e32 v[8:9], v[56:57]
	v_mov_b64_e32 v[10:11], v[58:59]
	v_mov_b64_e32 v[12:13], v[60:61]
	v_mov_b64_e32 v[14:15], v[62:63]

	.amdhsa_kernel _Z11attn_kernelPKDF16_S0_PDF16_P15HIP_vector_typeIfLj2EE
		.amdhsa_group_segment_fixed_size 81920
		.amdhsa_private_segment_fixed_size 0
		.amdhsa_kernarg_size 32
		.amdhsa_user_sgpr_count 2
		.amdhsa_user_sgpr_dispatch_ptr 0
		.amdhsa_user_sgpr_queue_ptr 0
		.amdhsa_user_sgpr_kernarg_segment_ptr 1
		.amdhsa_user_sgpr_dispatch_id 0
		.amdhsa_user_sgpr_kernarg_preload_length 0
		.amdhsa_user_sgpr_kernarg_preload_offset 0
		.amdhsa_user_sgpr_private_segment_size 0
		.amdhsa_uses_dynamic_stack 0
		.amdhsa_enable_private_segment 0
		.amdhsa_system_sgpr_workgroup_id_x 1
		.amdhsa_system_sgpr_workgroup_id_y 1
		.amdhsa_system_sgpr_workgroup_id_z 1
		.amdhsa_system_sgpr_workgroup_info 0
		.amdhsa_system_vgpr_workitem_id 0
		.amdhsa_next_free_vgpr 244
		.amdhsa_next_free_sgpr 40
		.amdhsa_accum_offset 244
		.amdhsa_reserve_vcc 1
		.amdhsa_float_round_mode_32 0
		.amdhsa_float_round_mode_16_64 0
		.amdhsa_float_denorm_mode_32 3
		.amdhsa_float_denorm_mode_16_64 3
		.amdhsa_dx10_clamp 1
		.amdhsa_ieee_mode 1
		.amdhsa_fp16_overflow 0
		.amdhsa_tg_split 0
		.amdhsa_exception_fp_ieee_invalid_op 0
		.amdhsa_exception_fp_denorm_src 0
		.amdhsa_exception_fp_ieee_div_zero 0
		.amdhsa_exception_fp_ieee_overflow 0
		.amdhsa_exception_fp_ieee_underflow 0
		.amdhsa_exception_fp_ieee_inexact 0
		.amdhsa_exception_int_div_zero 0
	.end_amdhsa_kernel

amdhsa.kernels:
  - .agpr_count:     32
    .args:
      - .actual_access:  read_only
        .address_space:  global
        .offset:         0
        .size:           8
        .value_kind:     global_buffer
      - .actual_access:  read_only
        .address_space:  global
        .offset:         8
        .size:           8
        .value_kind:     global_buffer
      - .actual_access:  read_only
        .address_space:  global
        .offset:         16
        .size:           8
        .value_kind:     global_buffer
      - .actual_access:  read_only
        .address_space:  global
        .offset:         24
        .size:           8
        .value_kind:     global_buffer
      - .actual_access:  write_only
        .address_space:  global
        .offset:         32
        .size:           8
        .value_kind:     global_buffer
      - .actual_access:  write_only
        .address_space:  global
        .offset:         40
        .size:           8
        .value_kind:     global_buffer
      - .actual_access:  read_only
        .address_space:  global
        .offset:         48
        .size:           8
        .value_kind:     global_buffer
      - .actual_access:  write_only
        .address_space:  global
        .offset:         56
        .size:           8
        .value_kind:     global_buffer
    .group_segment_fixed_size: 34816
    .kernarg_segment_align: 8
    .kernarg_segment_size: 64
    .language:       OpenCL C
    .language_version:
      - 2
      - 0
    .max_flat_workgroup_size: 256
    .name:           _Z11prep_kernelPKfS0_S0_S0_PDF16_S1_S0_S1_
    .private_segment_fixed_size: 0
    .sgpr_count:     30
    .sgpr_spill_count: 0
    .symbol:         _Z11prep_kernelPKfS0_S0_S0_PDF16_S1_S0_S1_.kd
    .uniform_work_group_size: 1
    .uses_dynamic_stack: false
    .vgpr_count:     220
    .vgpr_spill_count: 0
    .wavefront_size: 64
  - .agpr_count:     0
    .args:
      - .actual_access:  read_only
        .address_space:  global
        .offset:         0
        .size:           8
        .value_kind:     global_buffer
      - .address_space:  global
        .offset:         8
        .size:           8
        .value_kind:     global_buffer
      - .actual_access:  write_only
        .address_space:  global
        .offset:         16
        .size:           8
        .value_kind:     global_buffer
      - .actual_access:  write_only
        .address_space:  global
        .offset:         24
        .size:           8
        .value_kind:     global_buffer
    .group_segment_fixed_size: 81920
    .kernarg_segment_align: 8
    .kernarg_segment_size: 32
    .language:       OpenCL C
    .language_version:
      - 2
      - 0
    .max_flat_workgroup_size: 512
    .name:           _Z11attn_kernelPKDF16_S0_PDF16_P15HIP_vector_typeIfLj2EE
    .private_segment_fixed_size: 0
    .sgpr_count:     46
    .sgpr_spill_count: 0
    .symbol:         _Z11attn_kernelPKDF16_S0_PDF16_P15HIP_vector_typeIfLj2EE.kd
    .uniform_work_group_size: 1
    .uses_dynamic_stack: false
    .vgpr_count:     244
    .vgpr_spill_count: 0
    .wavefront_size: 64
  - .agpr_count:     0
    .args:
      - .actual_access:  read_only
        .address_space:  global
        .offset:         0
        .size:           8
        .value_kind:     global_buffer
      - .actual_access:  read_only
        .address_space:  global
        .offset:         8
        .size:           8
        .value_kind:     global_buffer
      - .actual_access:  read_only
        .address_space:  global
        .offset:         16
        .size:           8
        .value_kind:     global_buffer
      - .actual_access:  read_only
        .address_space:  global
        .offset:         24
        .size:           8
        .value_kind:     global_buffer
      - .actual_access:  write_only
        .address_space:  global
        .offset:         32
        .size:           8
        .value_kind:     global_buffer
    .group_segment_fixed_size: 50176
    .kernarg_segment_align: 8
    .kernarg_segment_size: 40
    .language:       OpenCL C
    .language_version:
      - 2
      - 0
    .max_flat_workgroup_size: 256
    .name:           _Z19combine_proj_kernelPKDF16_PK15HIP_vector_typeIfLj2EES0_PKfPf
    .private_segment_fixed_size: 0
    .sgpr_count:     50
    .sgpr_spill_count: 0
    .symbol:         _Z19combine_proj_kernelPKDF16_PK15HIP_vector_typeIfLj2EES0_PKfPf.kd
    .uniform_work_group_size: 1
    .uses_dynamic_stack: false
    .vgpr_count:     220
    .vgpr_spill_count: 0
    .wavefront_size: 64
